# v2_count_in_data
# speedup vs baseline: 1.0361x; 1.0181x over previous
.LBB1_50:
	s_or_b64 exec, exec, s[0:1]
	v_and_b32_e32 v1, 31, v0
	v_lshrrev_b32_e32 v24, 8, v0
	v_mad_u32_u24 v19, v24, 42, v1
	v_min_u32_e32 v20, 0x53, v19
	v_lshrrev_b32_e32 v18, 5, v193
	s_movk_i32 s64, 0x110
	v_mul_u32_u24_e32 v25, 0x110, v20
	v_min_u32_e32 v20, 62, v19
	v_lshlrev_b32_e32 v206, 6, v189
	v_mov_b32_e32 v66, 0
	v_mul_u32_u24_e32 v26, 0x110, v20
	v_lshlrev_b32_e32 v204, 4, v18
	v_mad_u32_u24 v22, v19, s64, v206
	v_lshlrev_b32_e32 v27, 3, v18
	v_lshlrev_b32_e32 v18, 1, v183
	v_mov_b32_e32 v19, v66
	v_lshlrev_b32_e32 v20, 10, v185
	v_lshl_add_u64 v[18:19], s[30:31], 0, v[18:19]
	v_and_b32_e32 v20, 0x1000, v20
	v_mov_b32_e32 v21, v66
	v_lshl_add_u64 v[18:19], v[18:19], 0, v[20:21]
	v_mov_b32_e32 v183, v66
	v_lshl_add_u64 v[18:19], v[18:19], 0, v[182:183]
	s_mov_b64 s[6:7], 0x48000
	v_lshl_add_u64 v[208:209], v[18:19], 0, s[6:7]
	v_lshrrev_b32_e32 v18, 2, v0
	v_and_b32_e32 v29, 8, v18
	v_mul_u32_u24_e32 v18, 0x3000, v189
	v_lshlrev_b32_e32 v210, 2, v193
	v_or_b32_e32 v18, v18, v210
	v_add_u32_e32 v221, 0x15a80, v18
	v_lshlrev_b32_e32 v18, 6, v193
	v_and_b32_e32 v20, 0xe00, v18
	s_add_u32 s34, s18, 0xc000
	s_movk_i32 s3, 0xff
	v_add_u32_e32 v19, 0x25a80, v210
	v_and_b32_e32 v224, 0x800, v18
	v_or_b32_e32 v225, 0x6600, v20
	v_or_b32_e32 v226, 0x7600, v20
	v_or_b32_e32 v227, 0x8600, v20
	v_or_b32_e32 v228, 0x9600, v20
	v_or_b32_e32 v229, 0x600, v20
	v_or_b32_e32 v230, 0x1600, v20
	v_or_b32_e32 v231, 0x2600, v20
	v_or_b32_e32 v232, 0x3600, v20
	v_or_b32_e32 v233, 0x4600, v20
	v_or_b32_e32 v234, 0x5600, v20
	v_lshlrev_b32_e32 v18, 8, v189
	v_lshlrev_b32_e32 v20, 2, v0
	s_addc_u32 s35, s19, 0
	v_cmp_lt_u32_e64 s[6:7], s3, v0
	v_and_b32_e32 v32, 0x7c, v20
	s_lshl_b32 s3, s2, 3
	v_add_u32_e32 v236, v19, v18
	s_lshl_b32 s2, s2, 5
	v_lshlrev_b32_e32 v18, 14, v185
	v_mov_b32_e32 v19, v66
	v_lshlrev_b32_e32 v20, 15, v189
	v_add_u32_e32 v28, 0x10140, v22
	v_add_u32_e32 v30, 0x11790, v22
	s_and_b32 s67, s3, 0x700
	s_and_b32 s2, s2, 0x1f00
	v_lshl_add_u64 v[18:19], s[30:31], 0, v[18:19]
	v_lshl_add_u64 v[20:21], s[30:31], 0, v[20:21]
	v_lshlrev_b32_e32 v22, 14, v24
	v_mov_b32_e32 v23, v66
	s_add_u32 s38, s34, s2
	v_lshl_add_u64 v[18:19], v[18:19], 0, v[182:183]
	s_mov_b64 s[2:3], 0x60000
	v_lshl_add_u64 v[20:21], v[20:21], 0, v[22:23]
	v_or_b32_e32 v220, v212, v1
	v_lshl_add_u64 v[212:213], v[18:19], 0, s[2:3]
	v_lshl_add_u64 v[20:21], v[20:21], 0, v[182:183]
	s_mov_b64 s[2:3], 0xc0000
	v_lshlrev_b32_e32 v33, 7, v185
	v_lshl_add_u64 v[214:215], v[20:21], 0, s[2:3]
	v_or_b32_e32 v23, 64, v1
	s_movk_i32 s69, 0x410
	v_mov_b32_e32 v20, 0x10140
	v_or_b32_e32 v237, v33, v32
	v_and_b32_e32 v18, 0x1c0, v0
	v_or_b32_e32 v22, v27, v33
	v_mad_u32_u24 v33, v23, s69, v20
	v_lshlrev_b32_e32 v20, 2, v32
	v_mov_b32_e32 v21, v66
	v_or_b32_e32 v31, 0x10140, v204
	v_lshlrev_b32_e32 v18, 2, v18
	v_mov_b32_e32 v19, v66
	s_movk_i32 s68, 0x54
	v_lshl_add_u64 v[216:217], s[26:27], 0, v[20:21]
	v_or_b32_e32 v20, 32, v1
	v_min_i32_e32 v21, 0x53, v23
	s_mov_b32 s37, 0
	v_lshl_or_b32 v207, v24, 7, v31
	v_cmp_eq_u32_e64 s[8:9], 1, v24
	v_lshlrev_b32_e32 v222, 2, v220
	v_lshl_add_u64 v[18:19], s[16:17], 0, v[18:19]
	v_cmp_gt_u32_e64 s[12:13], s68, v23
	v_lshl_or_b32 v24, v24, 9, v31
	v_mul_u32_u24_e32 v20, 0x110, v20
	v_mul_u32_u24_e32 v23, 0x110, v21
	v_mul_u32_u24_e32 v31, 0x410, v1
	v_mul_u32_u24_e32 v21, 0x410, v21
	v_mov_b32_e32 v205, v66
	s_mov_b32 s16, 0x18618618
	v_cmp_gt_u32_e64 s[0:1], 32, v193
	v_cmp_lt_u32_e64 s[14:15], 31, v193
	v_cmp_gt_u32_e64 s[4:5], 21, v1
	s_movk_i32 s65, 0x1000
	s_movk_i32 s66, 0x3000
	v_add_u32_e32 v223, 0x25680, v222
	v_lshl_or_b32 v235, v189, 7, v32
	v_cmp_eq_u32_e64 s[10:11], 0, v193
	s_addc_u32 s39, s35, 0
	v_mul_u32_u24_e32 v238, 0x110, v1
	v_add_u32_e32 v239, 0x10140, v22
	s_add_i32 s70, s33, 16
	s_add_i32 s71, s33, 32
	s_add_i32 s72, s33, 48
	s_add_i32 s73, s33, 64
	s_add_i32 s74, s33, 0x50
	v_lshl_add_u64 v[218:219], v[18:19], 0, v[204:205]
	v_add_u32_e32 v205, v25, v184
	v_add_u32_e32 v240, v26, v204
	v_add_u32_e32 v241, v207, v20
	v_add_u32_e32 v242, v207, v23
	s_movk_i32 s75, 0x2000
	s_movk_i32 s76, 0x100
	s_movk_i32 s77, 0xffc0
	s_mov_b32 s17, 0x3f086186
	s_mov_b32 s78, 0xf800000
	v_mov_b32_e32 v243, 0x260
	s_movk_i32 s79, 0x44
	v_add_u32_e32 v244, v33, v22
	v_add_u32_e32 v245, v24, v31
	v_add_u32_e32 v246, v24, v21
	v_add_u32_e32 v247, v28, v27
	v_add_u32_e32 v248, v30, v29
	v_mov_b32_e32 v249, 0x25680
	s_mov_b32 s36, s37
	s_waitcnt lgkmcnt(0)
	s_barrier
	s_branch .LBB1_53

.LBB1_83:
	s_or_saveexec_b64 s[26:27], s[26:27]
	v_add_u32_e32 v185, v237, v224
	v_add_u32_e32 v191, v237, v229
	v_add_u32_e32 v190, v237, v230
	v_add_u32_e32 v189, v237, v231
	v_add_u32_e32 v188, v237, v232
	v_add_u32_e32 v187, v237, v233
	v_add_u32_e32 v186, v237, v234
	v_lshlrev_b32_e32 v172, 2, v206
	s_xor_b64 exec, exec, s[26:27]
	s_cbranch_execz .LBB1_88
	ds_read_b32 v3, v236
	v_mul_u32_u24_e32 v4, 37, v1
	v_lshrrev_b32_e32 v4, 8, v4
	v_mul_u32_u24_e32 v5, 7, v4
	v_sub_u32_e32 v5, v1, v5
	v_lshlrev_b32_e32 v6, 6, v4
	v_lshl_add_u32 v6, v5, 3, v6
	v_bfe_u32 v7, v0, 5, 1
	v_lshl_add_u32 v6, v7, 2, v6
	v_lshlrev_b32_e32 v8, 6, v1
	v_add_u32_e32 v8, 0xfffff938, v8
	v_cmp_lt_u32_e32 vcc, 27, v1
	v_readfirstlane_b32 s42, v206
	s_mul_i32 s43, s36, 0x5000
	s_lshr_b32 s40, s67, 8
	s_mul_i32 s40, s40, 0x500
	s_add_i32 s43, s43, s40
	s_mul_i32 s42, s42, 5
	s_add_i32 s43, s43, s42
	s_add_u32 s40, s18, s43
	s_addc_u32 s41, s19, 0
	v_cndmask_b32_e32 v9, v6, v8, vcc
	s_waitcnt lgkmcnt(0)
	v_add_f32_e32 v2, v2, v3
	v_cndmask_b32_e64 v10, v2, 1.0, vcc
	v_mov_b32_e32 v16, v6
	v_mov_b32_e32 v17, v2
	s_movk_i32 s42, 0x138
	v_writelane_b32 v16, s42, 0
	v_writelane_b32 v17, 1.0, 0
	s_mov_b64 s[44:45], exec
	s_mov_b32 exec_lo, -1
	s_mov_b32 exec_hi, 0xfffffff
	global_atomic_add_f32 v9, v10, s[40:41]
	s_mov_b32 exec_lo, 0xf0000001
	s_mov_b32 exec_hi, 0xf0000000
	global_atomic_add_f32 v16, v17, s[40:41]
	s_mov_b64 exec, s[44:45]
	ds_write2st64_b32 v185, v50, v51 offset1:2
	ds_write_b32 v185, v52 offset:1024
	ds_write_b32 v191, v53
	ds_write2st64_b32 v185, v54, v55 offset0:16 offset1:18
	ds_write_b32 v185, v56 offset:5120
	ds_write_b32 v190, v57
	ds_write2st64_b32 v185, v58, v59 offset0:32 offset1:34
	ds_write_b32 v185, v60 offset:9216
	ds_write_b32 v189, v61
	ds_write2st64_b32 v185, v62, v63 offset0:48 offset1:50
	ds_write_b32 v185, v69 offset:13312
	ds_write_b32 v188, v65
	ds_write2st64_b32 v185, v70, v71 offset0:64 offset1:66
	ds_write_b32 v185, v74 offset:17408
	ds_write_b32 v187, v77
	ds_write2st64_b32 v185, v11, v12 offset0:80 offset1:82
	ds_write_b32 v185, v13 offset:21504
	ds_write_b32 v186, v15
.LBB1_88:
	s_or_b64 exec, exec, s[26:27]
	v_mov_b32_e32 v2, v0
	s_waitcnt lgkmcnt(0)
	s_barrier
	s_lshl_b32 s30, s36, 1
	v_ashrrev_i32_e32 v3, 5, v2
	v_lshlrev_b32_e32 v2, 4, v2
	v_and_b32_e32 v2, 0x1f0, v2
	v_min_i32_e32 v4, 0x53, v3
	v_lshl_or_b32 v4, v4, 9, v2
	v_min_i32_e32 v5, 0x43, v3
	v_lshl_or_b32 v5, v5, 9, v2
	ds_read_b128 v[54:57], v4
	ds_read_b128 v[50:53], v5 offset:8192
	v_min_i32_e32 v4, 51, v3
	v_lshl_or_b32 v4, v4, 9, v2
	v_min_i32_e32 v5, 35, v3
	v_lshl_or_b32 v5, v5, 9, v2
	ds_read_b128 v[46:49], v4 offset:16384
	ds_read_b128 v[42:45], v5 offset:24576
	v_min_i32_e32 v4, 19, v3
	v_lshl_or_b32 v4, v4, 9, v2
	v_min_i32_e32 v3, 3, v3
	v_lshl_or_b32 v2, v3, 9, v2
	ds_read_b128 v[38:41], v4 offset:32768
	ds_read_b128 v[34:37], v2 offset:40960
	s_lshl_b64 s[26:27], s[36:37], 17
	v_lshl_add_u64 v[2:3], v[212:213], 0, s[26:27]
	v_add_co_u32_e32 v4, vcc, s65, v2
	global_load_dwordx4 v[100:103], v[2:3], off
	global_load_dwordx4 v[92:95], v[2:3], off offset:1024
	global_load_dwordx4 v[88:91], v[2:3], off offset:2048
	global_load_dwordx4 v[80:83], v[2:3], off offset:3072
	v_addc_co_u32_e32 v5, vcc, 0, v3, vcc
	v_add_co_u32_e32 v6, vcc, s75, v2
	s_lshl_b32 s26, s36, 9
	s_nop 0
	v_addc_co_u32_e32 v7, vcc, 0, v3, vcc
	v_add_co_u32_e32 v2, vcc, s66, v2
	s_mov_b32 s27, s37
	s_nop 0
	v_addc_co_u32_e32 v3, vcc, 0, v3, vcc
	v_lshl_add_u64 v[14:15], s[26:27], 2, v[218:219]
	global_load_dwordx4 v[84:87], v[4:5], off offset:1024
	global_load_dwordx4 v[76:79], v[4:5], off offset:2048
	global_load_dwordx4 v[96:99], v[6:7], off offset:-4096
	global_load_dwordx4 v[128:131], v[6:7], off
	global_load_dwordx4 v[124:127], v[6:7], off offset:1024
	global_load_dwordx4 v[120:123], v[6:7], off offset:2048
	global_load_dwordx4 v[112:115], v[6:7], off offset:3072
	global_load_dwordx4 v[68:71], v[4:5], off offset:3072
	global_load_dwordx4 v[116:119], v[2:3], off
	global_load_dwordx4 v[108:111], v[2:3], off offset:1024
	global_load_dwordx4 v[104:107], v[2:3], off offset:2048
	global_load_dwordx4 v[72:75], v[2:3], off offset:3072
	global_load_dwordx4 v[18:21], v[14:15], off offset:1536
	global_load_dwordx4 v[22:25], v[14:15], off offset:1568
	s_nop 0
	global_load_dwordx4 v[2:5], v[14:15], off offset:1664
	global_load_dwordx4 v[6:9], v[14:15], off offset:1696
	global_load_dwordx4 v[26:29], v[14:15], off offset:1600
	global_load_dwordx4 v[30:33], v[14:15], off offset:1632
	global_load_dwordx4 v[10:13], v[14:15], off offset:1728
	s_nop 0
	global_load_dwordx4 v[14:17], v[14:15], off offset:1760
	v_mov_b32_e32 v58, v0
	s_or_b32 s80, s30, 1
	s_lshl_b32 s26, s36, 7
	s_nop 0
	v_cmp_gt_i32_e32 vcc, s76, v58
	s_and_saveexec_b64 s[30:31], vcc
	s_cbranch_execz .LBB1_126
	s_lshl_b64 s[40:41], s[26:27], 2
	s_add_u32 s40, s22, s40
	s_addc_u32 s41, s23, s41
	v_and_b32_e32 v58, 63, v0
	v_lshrrev_b32_e32 v64, 6, v0
	v_lshrrev_b32_e32 v59, 3, v58
	v_and_b32_e32 v60, 7, v58
	v_readfirstlane_b32 s52, v64
	v_min_u32_e32 v61, 4, v59
	v_lshlrev_b32_e32 v62, 6, v61
	v_lshl_add_u32 v62, v60, 3, v62
	v_mul_u32_u24_e32 v63, 7, v61
	v_add_u32_e32 v63, v63, v60
	v_cmp_gt_u32_e64 s[46:47], 5, v59
	v_cmp_gt_u32_e64 s[48:49], 7, v60
	v_cmp_gt_u32_e32 vcc, 32, v63
	v_cmp_eq_u32_e64 s[50:51], 7, v60
	s_and_b64 s[46:47], s[46:47], s[48:49]
	s_and_b64 s[46:47], s[46:47], vcc
	v_min_u32_e32 v63, 31, v63
	v_lshl_add_u32 v63, v64, 5, v63
	v_lshlrev_b32_e32 v65, 2, v63
	global_load_dword v132, v65, s[40:41]
	v_lshl_add_u32 v133, v63, 2, v249
	s_mul_i32 s52, s52, 0x140
	s_mul_i32 s53, s36, 0x5000
	s_add_i32 s53, s53, s52
	s_add_u32 s42, s18, s53
	s_addc_u32 s43, s19, 0
	s_add_u32 s44, s42, 0x1400
	s_addc_u32 s45, s43, 0
	s_mov_b32 s82, 0x10000
	s_mov_b32 s81, 0x43800000
.Lgw1_poll:
	global_load_dwordx2 v[134:135], v62, s[42:43] sc1
	global_load_dwordx2 v[136:137], v62, s[42:43] offset:1280 sc1
	global_load_dwordx2 v[138:139], v62, s[42:43] offset:2560 sc1
	global_load_dwordx2 v[140:141], v62, s[42:43] offset:3840 sc1
	global_load_dwordx2 v[142:143], v62, s[44:45] sc1
	global_load_dwordx2 v[144:145], v62, s[44:45] offset:1280 sc1
	global_load_dwordx2 v[146:147], v62, s[44:45] offset:2560 sc1
	global_load_dwordx2 v[148:149], v62, s[44:45] offset:3840 sc1
	s_waitcnt vmcnt(0)
	v_add_f32_e32 v150, v134, v136
	v_add_f32_e32 v150, v150, v138
	v_add_f32_e32 v150, v150, v140
	v_add_f32_e32 v150, v150, v142
	v_add_f32_e32 v150, v150, v144
	v_add_f32_e32 v150, v150, v146
	v_add_f32_e32 v150, v150, v148
	v_cmp_eq_f32_e32 vcc, s81, v150
	s_orn2_b64 vcc, vcc, s[50:51]
	s_cmp_eq_u64 vcc, exec
	s_cbranch_scc1 .Lgw1_done
	s_sleep 1
	s_add_i32 s82, s82, -1
	s_cmp_lg_u32 s82, 0
	s_cbranch_scc1 .Lgw1_poll
.Lgw1_done:
	v_cvt_f64_f32_e32 v[58:59], v134
	v_cvt_f64_f32_e32 v[60:61], v135
	v_cvt_f64_f32_e32 v[64:65], v136
	v_cvt_f64_f32_e32 v[152:153], v137
	v_add_f64 v[58:59], v[58:59], v[64:65]
	v_add_f64 v[60:61], v[60:61], v[152:153]
	v_cvt_f64_f32_e32 v[64:65], v138
	v_cvt_f64_f32_e32 v[152:153], v139
	v_add_f64 v[58:59], v[58:59], v[64:65]
	v_add_f64 v[60:61], v[60:61], v[152:153]
	v_cvt_f64_f32_e32 v[64:65], v140
	v_cvt_f64_f32_e32 v[152:153], v141
	v_add_f64 v[58:59], v[58:59], v[64:65]
	v_add_f64 v[60:61], v[60:61], v[152:153]
	v_cvt_f64_f32_e32 v[64:65], v142
	v_cvt_f64_f32_e32 v[152:153], v143
	v_add_f64 v[58:59], v[58:59], v[64:65]
	v_add_f64 v[60:61], v[60:61], v[152:153]
	v_cvt_f64_f32_e32 v[64:65], v144
	v_cvt_f64_f32_e32 v[152:153], v145
	v_add_f64 v[58:59], v[58:59], v[64:65]
	v_add_f64 v[60:61], v[60:61], v[152:153]
	v_cvt_f64_f32_e32 v[64:65], v146
	v_cvt_f64_f32_e32 v[152:153], v147
	v_add_f64 v[58:59], v[58:59], v[64:65]
	v_add_f64 v[60:61], v[60:61], v[152:153]
	v_cvt_f64_f32_e32 v[64:65], v148
	v_cvt_f64_f32_e32 v[152:153], v149
	v_add_f64 v[58:59], v[58:59], v[64:65]
	v_add_f64 v[60:61], v[60:61], v[152:153]
	v_mul_f64 v[58:59], v[58:59], s[16:17]
	v_mul_f64 v[64:65], v[58:59], v[58:59]
	v_fma_f64 v[60:61], v[60:61], s[16:17], -v[64:65]
	v_cvt_f32_f64_e32 v60, v[60:61]
	v_cvt_f32_f64_e32 v58, v[58:59]
	v_add_f32_e32 v60, 0x3727c5ac, v60
	v_rsq_f32_e32 v60, v60
	s_nop 0
	v_mul_f32_e32 v60, v132, v60
	s_and_b64 exec, exec, s[46:47]
	ds_write2st64_b32 v133, v58, v60 offset1:2

.LBB1_164:
	s_andn2_saveexec_b64 s[30:31], s[30:31]
	s_cbranch_execz .LBB1_169
	ds_read_b32 v3, v236
	v_mul_u32_u24_e32 v4, 37, v1
	v_lshrrev_b32_e32 v4, 8, v4
	v_mul_u32_u24_e32 v5, 7, v4
	v_sub_u32_e32 v5, v1, v5
	v_lshlrev_b32_e32 v6, 6, v4
	v_lshl_add_u32 v6, v5, 3, v6
	v_bfe_u32 v7, v0, 5, 1
	v_lshl_add_u32 v6, v7, 2, v6
	v_lshlrev_b32_e32 v8, 6, v1
	v_add_u32_e32 v8, 0xfffff938, v8
	v_cmp_lt_u32_e32 vcc, 27, v1
	v_readfirstlane_b32 s42, v206
	s_mul_i32 s43, s36, 0x5000
	s_addk_i32 s43, 0x2800
	s_lshr_b32 s40, s67, 8
	s_mul_i32 s40, s40, 0x500
	s_add_i32 s43, s43, s40
	s_mul_i32 s42, s42, 5
	s_add_i32 s43, s43, s42
	s_add_u32 s40, s18, s43
	s_addc_u32 s41, s19, 0
	v_cndmask_b32_e32 v9, v6, v8, vcc
	s_waitcnt lgkmcnt(0)
	v_add_f32_e32 v2, v2, v3
	v_cndmask_b32_e64 v10, v2, 1.0, vcc
	v_mov_b32_e32 v16, v6
	v_mov_b32_e32 v17, v2
	s_movk_i32 s42, 0x138
	v_writelane_b32 v16, s42, 0
	v_writelane_b32 v17, 1.0, 0
	s_mov_b64 s[44:45], exec
	s_mov_b32 exec_lo, -1
	s_mov_b32 exec_hi, 0xfffffff
	global_atomic_add_f32 v9, v10, s[40:41]
	s_mov_b32 exec_lo, 0xf0000001
	s_mov_b32 exec_hi, 0xf0000000
	global_atomic_add_f32 v16, v17, s[40:41]
	s_mov_b64 exec, s[44:45]
	ds_write2st64_b32 v185, v50, v51 offset1:2
	ds_write_b32 v185, v52 offset:1024
	ds_write_b32 v191, v53
	ds_write2st64_b32 v185, v54, v55 offset0:16 offset1:18
	ds_write_b32 v185, v56 offset:5120
	ds_write_b32 v190, v57
	ds_write2st64_b32 v185, v58, v59 offset0:32 offset1:34
	ds_write_b32 v185, v60 offset:9216
	ds_write_b32 v189, v61
	ds_write2st64_b32 v185, v62, v63 offset0:48 offset1:50
	ds_write_b32 v185, v69 offset:13312
	ds_write_b32 v188, v65
	ds_write2st64_b32 v185, v70, v71 offset0:64 offset1:66
	ds_write_b32 v185, v74 offset:17408
	ds_write_b32 v187, v77
	ds_write2st64_b32 v185, v11, v12 offset0:80 offset1:82
	ds_write_b32 v185, v13 offset:21504
	ds_write_b32 v186, v15
.LBB1_169:
	s_or_b64 exec, exec, s[30:31]
	v_mov_b32_e32 v2, v0
	s_waitcnt lgkmcnt(0)
	s_barrier
	s_nop 0
	v_ashrrev_i32_e32 v3, 5, v2
	v_lshlrev_b32_e32 v2, 4, v2
	v_and_b32_e32 v2, 0x1f0, v2
	v_min_i32_e32 v4, 0x53, v3
	v_lshl_or_b32 v4, v4, 9, v2
	v_min_i32_e32 v5, 0x43, v3
	v_lshl_or_b32 v5, v5, 9, v2
	ds_read_b128 v[42:45], v4
	ds_read_b128 v[38:41], v5 offset:8192
	v_min_i32_e32 v4, 51, v3
	v_lshl_or_b32 v4, v4, 9, v2
	v_min_i32_e32 v5, 35, v3
	v_lshl_or_b32 v5, v5, 9, v2
	ds_read_b128 v[34:37], v4 offset:16384
	ds_read_b128 v[30:33], v5 offset:24576
	v_min_i32_e32 v4, 19, v3
	v_lshl_or_b32 v4, v4, 9, v2
	v_min_i32_e32 v3, 3, v3
	v_lshl_or_b32 v2, v3, 9, v2
	ds_read_b128 v[22:25], v4 offset:32768
	ds_read_b128 v[18:21], v2 offset:40960
	s_add_i32 s80, s36, 1
	s_cmp_lg_u32 s36, 2
	s_cselect_b64 s[30:31], -1, 0
	s_and_b64 s[40:41], s[30:31], exec
	s_cselect_b32 s42, s80, 2
	s_lshl_b32 s40, s42, 15
	s_mov_b32 s41, s37
	v_lshl_add_u64 v[2:3], v[196:197], 0, s[40:41]
	v_lshl_add_u64 v[4:5], v[198:199], 0, s[40:41]
	v_lshl_add_u64 v[6:7], v[200:201], 0, s[40:41]
	global_load_dwordx4 v[116:119], v[2:3], off
	global_load_dwordx4 v[120:123], v[2:3], off offset:1024
	global_load_dwordx4 v[112:115], v[4:5], off
	global_load_dwordx4 v[100:103], v[4:5], off offset:1024
	global_load_dwordx4 v[96:99], v[6:7], off
	global_load_dwordx4 v[76:79], v[6:7], off offset:1024
	global_load_dwordx4 v[124:127], v[2:3], off offset:2048
	global_load_dwordx4 v[128:131], v[2:3], off offset:3072
	global_load_dwordx4 v[104:107], v[4:5], off offset:2048
	global_load_dwordx4 v[108:111], v[4:5], off offset:3072
	global_load_dwordx4 v[72:75], v[6:7], off offset:2048
	global_load_dwordx4 v[68:71], v[6:7], off offset:3072
	v_add_co_u32_e32 v2, vcc, s65, v2
	s_lshl_b32 s40, s42, 7
	s_nop 0
	v_addc_co_u32_e32 v3, vcc, 0, v3, vcc
	v_add_co_u32_e32 v4, vcc, s65, v4
	v_lshl_add_u64 v[14:15], s[40:41], 2, v[202:203]
	s_nop 0
	v_addc_co_u32_e32 v5, vcc, 0, v5, vcc
	v_add_co_u32_e32 v6, vcc, s65, v6
	s_nop 1
	v_addc_co_u32_e32 v7, vcc, 0, v7, vcc
	global_load_dwordx4 v[148:151], v[2:3], off
	global_load_dwordx4 v[152:155], v[2:3], off offset:1024
	global_load_dwordx4 v[132:135], v[4:5], off
	global_load_dwordx4 v[136:139], v[4:5], off offset:1024
	global_load_dwordx4 v[92:95], v[6:7], off
	global_load_dwordx4 v[84:87], v[6:7], off offset:1024
	global_load_dwordx4 v[156:159], v[2:3], off offset:2048
	global_load_dwordx4 v[160:163], v[2:3], off offset:3072
	global_load_dwordx4 v[140:143], v[4:5], off offset:2048
	global_load_dwordx4 v[144:147], v[4:5], off offset:3072
	global_load_dwordx4 v[88:91], v[6:7], off offset:2048
	global_load_dwordx4 v[80:83], v[6:7], off offset:3072
	s_nop 0
	global_load_dwordx4 v[2:5], v[14:15], off
	global_load_dwordx4 v[6:9], v[14:15], off offset:32
	global_load_dwordx4 v[10:13], v[14:15], off offset:64
	s_nop 0
	global_load_dwordx4 v[14:17], v[14:15], off offset:96
	s_nop 0
	global_load_dwordx4 v[26:29], v[216:217], off offset:1024
	v_mov_b32_e32 v46, v0
	s_nop 0
	v_cmp_gt_i32_e32 vcc, s76, v46
	s_and_saveexec_b64 s[40:41], vcc
	s_cbranch_execz .LBB1_207
	s_lshl_b64 s[26:27], s[26:27], 2
	s_add_u32 s26, s24, s26
	s_addc_u32 s27, s25, s27
	v_and_b32_e32 v46, 63, v0
	v_lshrrev_b32_e32 v52, 6, v0
	v_lshrrev_b32_e32 v47, 3, v46
	v_and_b32_e32 v48, 7, v46
	v_readfirstlane_b32 s52, v52
	v_min_u32_e32 v49, 4, v47
	v_lshlrev_b32_e32 v50, 6, v49
	v_lshl_add_u32 v50, v48, 3, v50
	v_mul_u32_u24_e32 v51, 7, v49
	v_add_u32_e32 v51, v51, v48
	v_cmp_gt_u32_e64 s[46:47], 5, v47
	v_cmp_gt_u32_e64 s[48:49], 7, v48
	v_cmp_gt_u32_e32 vcc, 32, v51
	v_cmp_eq_u32_e64 s[50:51], 7, v48
	s_and_b64 s[46:47], s[46:47], s[48:49]
	s_and_b64 s[46:47], s[46:47], vcc
	v_min_u32_e32 v51, 31, v51
	v_lshl_add_u32 v51, v52, 5, v51
	v_lshlrev_b32_e32 v53, 2, v51
	global_load_dword v54, v53, s[26:27]
	v_lshl_add_u32 v55, v51, 2, v249
	s_mul_i32 s52, s52, 0x140
	s_mul_i32 s53, s36, 0x5000
	s_addk_i32 s53, 0x2800
	s_add_i32 s53, s53, s52
	s_add_u32 s42, s18, s53
	s_addc_u32 s43, s19, 0
	s_add_u32 s44, s42, 0x1400
	s_addc_u32 s45, s43, 0
	s_mov_b32 s81, 0x10000
	s_mov_b32 s82, 0x43800000
.Lgw2_poll:
	global_load_dwordx2 v[56:57], v50, s[42:43] sc1
	global_load_dwordx2 v[58:59], v50, s[42:43] offset:1280 sc1
	global_load_dwordx2 v[60:61], v50, s[42:43] offset:2560 sc1
	global_load_dwordx2 v[62:63], v50, s[42:43] offset:3840 sc1
	global_load_dwordx2 v[64:65], v50, s[44:45] sc1
	global_load_dwordx2 v[164:165], v50, s[44:45] offset:1280 sc1
	global_load_dwordx2 v[166:167], v50, s[44:45] offset:2560 sc1
	global_load_dwordx2 v[168:169], v50, s[44:45] offset:3840 sc1
	s_waitcnt vmcnt(0)
	v_add_f32_e32 v170, v56, v58
	v_add_f32_e32 v170, v170, v60
	v_add_f32_e32 v170, v170, v62
	v_add_f32_e32 v170, v170, v64
	v_add_f32_e32 v170, v170, v164
	v_add_f32_e32 v170, v170, v166
	v_add_f32_e32 v170, v170, v168
	v_cmp_eq_f32_e32 vcc, s82, v170
	s_orn2_b64 vcc, vcc, s[50:51]
	s_cmp_eq_u64 vcc, exec
	s_cbranch_scc1 .Lgw2_done
	s_sleep 1
	s_add_i32 s81, s81, -1
	s_cmp_lg_u32 s81, 0
	s_cbranch_scc1 .Lgw2_poll
.Lgw2_done:
	v_cvt_f64_f32_e32 v[46:47], v56
	v_cvt_f64_f32_e32 v[48:49], v57
	v_cvt_f64_f32_e32 v[52:53], v58
	v_cvt_f64_f32_e32 v[172:173], v59
	v_add_f64 v[46:47], v[46:47], v[52:53]
	v_add_f64 v[48:49], v[48:49], v[172:173]
	v_cvt_f64_f32_e32 v[52:53], v60
	v_cvt_f64_f32_e32 v[172:173], v61
	v_add_f64 v[46:47], v[46:47], v[52:53]
	v_add_f64 v[48:49], v[48:49], v[172:173]
	v_cvt_f64_f32_e32 v[52:53], v62
	v_cvt_f64_f32_e32 v[172:173], v63
	v_add_f64 v[46:47], v[46:47], v[52:53]
	v_add_f64 v[48:49], v[48:49], v[172:173]
	v_cvt_f64_f32_e32 v[52:53], v64
	v_cvt_f64_f32_e32 v[172:173], v65
	v_add_f64 v[46:47], v[46:47], v[52:53]
	v_add_f64 v[48:49], v[48:49], v[172:173]
	v_cvt_f64_f32_e32 v[52:53], v164
	v_cvt_f64_f32_e32 v[172:173], v165
	v_add_f64 v[46:47], v[46:47], v[52:53]
	v_add_f64 v[48:49], v[48:49], v[172:173]
	v_cvt_f64_f32_e32 v[52:53], v166
	v_cvt_f64_f32_e32 v[172:173], v167
	v_add_f64 v[46:47], v[46:47], v[52:53]
	v_add_f64 v[48:49], v[48:49], v[172:173]
	v_cvt_f64_f32_e32 v[52:53], v168
	v_cvt_f64_f32_e32 v[172:173], v169
	v_add_f64 v[46:47], v[46:47], v[52:53]
	v_add_f64 v[48:49], v[48:49], v[172:173]
	v_mul_f64 v[46:47], v[46:47], s[16:17]
	v_mul_f64 v[52:53], v[46:47], v[46:47]
	v_fma_f64 v[48:49], v[48:49], s[16:17], -v[52:53]
	v_cvt_f32_f64_e32 v48, v[48:49]
	v_cvt_f32_f64_e32 v46, v[46:47]
	v_add_f32_e32 v48, 0x3727c5ac, v48
	v_rsq_f32_e32 v48, v48
	s_nop 0
	v_mul_f32_e32 v48, v54, v48
	s_and_b64 exec, exec, s[46:47]
	ds_write2st64_b32 v55, v46, v48 offset1:2
